# baseline (speedup 1.0000x reference)
.Lk_144:
	v_or_b32_e32 v46, 0x400, v54
	buffer_load_dwordx4 v[46:49], v46, s[4:7], 0 offen sc1
	ds_read_b128 v[50:53], v1
	v_mov_b32_e32 v66, 0
	v_add_u32_e32 v63, 0x800, v54
	s_mov_b32 s9, 0
	v_mov_b32_e32 v67, 0
	v_mov_b32_e32 v68, 0
	v_mov_b32_e32 v62, 0xc038aa3b
	s_mov_b32 s8, 0x4038aa3b
	v_mov_b32_e32 v65, 0
	v_mov_b32_e32 v64, v66
	s_setprio 2
	v_mov_b32_e32 v92, 0xc038aa3b
	v_mov_b32_e32 v93, 0xc038aa3b
	s_mov_b32 s8, 0x4038aa3b
	s_mov_b32 s9, 0
	v_mov_b32_e32 v64, 0
	v_mov_b32_e32 v65, 0
	v_mov_b32_e32 v66, 0
	v_mov_b32_e32 v67, 0
	v_mov_b32_e32 v68, 0
	v_mov_b32_e32 v116, v1
	v_mov_b32_e32 v117, v63
	s_mov_b32 s12, 0
	s_waitcnt lgkmcnt(0)
	s_setprio 2
	v_mfma_f32_16x16x32_f16 v[84:87], v[6:9], v[50:53], v[18:21]
	v_mfma_f32_16x16x32_f16 v[88:91], v[10:13], v[50:53], v[38:41]
	ds_read_b128 v[56:59], v75 offset:2048
	ds_read_b128 v[60:63], v75 offset:3072
	s_waitcnt vmcnt(1)
	v_mfma_f32_16x16x32_f16 v[84:87], v[2:5], v[42:45], v[84:87]
	v_mfma_f32_16x16x32_f16 v[88:91], v[14:17], v[42:45], v[88:91]
	s_waitcnt lgkmcnt(1)
	v_mfma_f32_16x16x32_f16 v[84:87], v[30:33], v[56:59], v[84:87]
	v_mfma_f32_16x16x32_f16 v[88:91], v[22:25], v[56:59], v[88:91]
	s_waitcnt lgkmcnt(0)
	v_mfma_f32_16x16x32_f16 v[84:87], v[34:37], v[60:63], v[84:87]
	v_mfma_f32_16x16x32_f16 v[88:91], v[26:29], v[60:63], v[88:91]
	s_nop 7
	v_exp_f32_e32 v94, v86
	v_exp_f32_e32 v95, v90
	v_exp_f32_e32 v96, v84
	v_exp_f32_e32 v97, v88
	v_exp_f32_e32 v98, v85
	v_exp_f32_e32 v99, v89
	s_setprio 0
	v_pk_add_f32 v[100:101], v[94:95], 1.0 op_sel_hi:[1,0]
	v_pk_fma_f32 v[102:103], v[94:95], s[8:9], v[92:93] op_sel_hi:[1,0,0]
	v_pk_fma_f32 v[100:101], v[96:97], v[100:101], v[100:101]
	v_pk_fma_f32 v[104:105], v[100:101], v[98:99], v[100:101]
	v_rcp_f32_e32 v104, v104
	v_rcp_f32_e32 v105, v105
	v_pk_fma_f32 v[102:103], v[102:103], v[98:99], v[102:103]
	v_pk_fma_f32 v[102:103], v[64:65], v[100:101], v[102:103]
	v_exp_f32_e32 v106, v87
	v_pk_mul_f32 v[64:65], v[102:103], v[104:105]
	v_exp_f32_e32 v108, v64
	v_exp_f32_e32 v109, v65
	v_exp_f32_e32 v107, v91
	v_pk_add_f32 v[110:111], v[108:109], 1.0 op_sel_hi:[1,0]
	v_pk_fma_f32 v[110:111], v[110:111], v[106:107], v[110:111]
	v_rcp_f32_e32 v110, v110
	v_rcp_f32_e32 v111, v111
	v_pk_add_f32 v[112:113], v[108:109], -1.0 op_sel_hi:[1,0]
	v_pk_mul_f32 v[112:113], v[112:113], v[110:111]
	v_cvt_pk_f16_f32 v114, v112, v113
	ds_write_b32 v81, v114 offset:0
	s_waitcnt lgkmcnt(0)
	global_load_dword v67, v66, s[0:1] sc1
	global_load_dword v68, v66, s[0:1] offset:4 sc1
	s_add_u32 s13, s12, 3
	s_min_u32 s13, s13, 450
	s_cmp_ge_u32 s14, s13
	s_cbranch_scc0 .Lca_slow_3
.Lca_ok_1:
	buffer_load_dwordx4 v[42:45], v117, s[4:7], 0 offen offset:0 sc1
	ds_read_b128 v[50:53], v116 offset:256
	s_setprio 0
	s_waitcnt vmcnt(3) lgkmcnt(0)
	s_setprio 2
	s_barrier
	v_mfma_f32_16x16x32_f16 v[84:87], v[6:9], v[50:53], v[18:21]
	v_mfma_f32_16x16x32_f16 v[88:91], v[10:13], v[50:53], v[38:41]
	ds_read_b128 v[56:59], v75 offset:0
	ds_read_b128 v[60:63], v75 offset:1024
	v_mfma_f32_16x16x32_f16 v[84:87], v[2:5], v[46:49], v[84:87]
	v_mfma_f32_16x16x32_f16 v[88:91], v[14:17], v[46:49], v[88:91]
	s_waitcnt lgkmcnt(1)
	v_mfma_f32_16x16x32_f16 v[84:87], v[30:33], v[56:59], v[84:87]
	v_mfma_f32_16x16x32_f16 v[88:91], v[22:25], v[56:59], v[88:91]
	s_waitcnt lgkmcnt(0)
	v_mfma_f32_16x16x32_f16 v[84:87], v[34:37], v[60:63], v[84:87]
	v_mfma_f32_16x16x32_f16 v[88:91], v[26:29], v[60:63], v[88:91]
	s_nop 7
	v_exp_f32_e32 v94, v86
	v_exp_f32_e32 v95, v90
	v_exp_f32_e32 v96, v84
	v_exp_f32_e32 v97, v88
	v_exp_f32_e32 v98, v85
	v_exp_f32_e32 v99, v89
	s_setprio 0
	v_pk_add_f32 v[100:101], v[94:95], 1.0 op_sel_hi:[1,0]
	v_pk_fma_f32 v[102:103], v[94:95], s[8:9], v[92:93] op_sel_hi:[1,0,0]
	v_pk_fma_f32 v[100:101], v[96:97], v[100:101], v[100:101]
	v_pk_fma_f32 v[104:105], v[100:101], v[98:99], v[100:101]
	v_rcp_f32_e32 v104, v104
	v_rcp_f32_e32 v105, v105
	v_pk_fma_f32 v[102:103], v[102:103], v[98:99], v[102:103]
	v_pk_fma_f32 v[102:103], v[64:65], v[100:101], v[102:103]
	v_exp_f32_e32 v106, v87
	v_pk_mul_f32 v[64:65], v[102:103], v[104:105]
	v_exp_f32_e32 v108, v64
	v_exp_f32_e32 v109, v65
	v_exp_f32_e32 v107, v91
	v_pk_add_f32 v[110:111], v[108:109], 1.0 op_sel_hi:[1,0]
	v_pk_fma_f32 v[110:111], v[110:111], v[106:107], v[110:111]
	v_rcp_f32_e32 v110, v110
	v_rcp_f32_e32 v111, v111
	v_pk_add_f32 v[112:113], v[108:109], -1.0 op_sel_hi:[1,0]
	v_pk_mul_f32 v[112:113], v[112:113], v[110:111]
	v_cvt_pk_f16_f32 v114, v112, v113
	ds_write_b32 v81, v114 offset:2048
	s_waitcnt lgkmcnt(0)
	s_add_u32 s13, s12, 4
	s_min_u32 s13, s13, 450
	s_cmp_ge_u32 s14, s13
	s_cbranch_scc0 .Lca_slow_6

.Lca_loop:
	s_setprio 2
	s_barrier
	v_mfma_f32_16x16x32_f16 v[84:87], v[6:9], v[50:53], v[18:21]
	v_mfma_f32_16x16x32_f16 v[88:91], v[10:13], v[50:53], v[38:41]
	ds_read_b128 v[56:59], v75 offset:2048
	ds_read_b128 v[60:63], v75 offset:3072
	v_mfma_f32_16x16x32_f16 v[84:87], v[2:5], v[42:45], v[84:87]
	v_mfma_f32_16x16x32_f16 v[88:91], v[14:17], v[42:45], v[88:91]
	s_waitcnt lgkmcnt(1)
	v_mfma_f32_16x16x32_f16 v[84:87], v[30:33], v[56:59], v[84:87]
	v_mfma_f32_16x16x32_f16 v[88:91], v[22:25], v[56:59], v[88:91]
	s_waitcnt lgkmcnt(0)
	v_mfma_f32_16x16x32_f16 v[84:87], v[34:37], v[60:63], v[84:87]
	v_mfma_f32_16x16x32_f16 v[88:91], v[26:29], v[60:63], v[88:91]
	s_nop 7
	v_exp_f32_e32 v94, v86
	v_exp_f32_e32 v95, v90
	v_exp_f32_e32 v96, v84
	v_exp_f32_e32 v97, v88
	v_exp_f32_e32 v98, v85
	v_exp_f32_e32 v99, v89
	s_setprio 0
	v_pk_add_f32 v[100:101], v[94:95], 1.0 op_sel_hi:[1,0]
	v_pk_fma_f32 v[102:103], v[94:95], s[8:9], v[92:93] op_sel_hi:[1,0,0]
	v_pk_fma_f32 v[100:101], v[96:97], v[100:101], v[100:101]
	v_pk_fma_f32 v[104:105], v[100:101], v[98:99], v[100:101]
	v_rcp_f32_e32 v104, v104
	v_rcp_f32_e32 v105, v105
	v_pk_fma_f32 v[102:103], v[102:103], v[98:99], v[102:103]
	v_pk_fma_f32 v[102:103], v[64:65], v[100:101], v[102:103]
	v_exp_f32_e32 v106, v87
	v_pk_mul_f32 v[64:65], v[102:103], v[104:105]
	v_exp_f32_e32 v108, v64
	v_exp_f32_e32 v109, v65
	v_exp_f32_e32 v107, v91
	v_pk_add_f32 v[110:111], v[108:109], 1.0 op_sel_hi:[1,0]
	v_pk_fma_f32 v[110:111], v[110:111], v[106:107], v[110:111]
	v_rcp_f32_e32 v110, v110
	v_rcp_f32_e32 v111, v111
	v_pk_add_f32 v[112:113], v[108:109], -1.0 op_sel_hi:[1,0]
	v_pk_mul_f32 v[112:113], v[112:113], v[110:111]
	v_cvt_pk_f16_f32 v114, v112, v113
	ds_write_b32 v81, v114 offset:0
	s_waitcnt lgkmcnt(0)
	v_min_f32_e32 v64, 0x42700000, v64
	v_min_f32_e32 v65, 0x42700000, v65
	v_readfirstlane_b32 s10, v67
	v_readfirstlane_b32 s11, v68
	global_load_dword v67, v66, s[0:1] sc1
	global_load_dword v68, v66, s[0:1] offset:4 sc1
	s_min_u32 s10, s10, s11
	s_max_u32 s14, s14, s10
	s_add_u32 s13, s12, 3
	s_min_u32 s13, s13, 450
	s_cmp_ge_u32 s14, s13
	s_cbranch_scc0 .Lca_slow_9

.Lca_ok_10:
	buffer_load_dwordx4 v[46:49], v117, s[4:7], 0 offen offset:1024 sc1
	ds_read_b128 v[50:53], v116 offset:512
	s_setprio 0
	s_waitcnt vmcnt(1) lgkmcnt(0)
	s_setprio 2
	s_barrier
	v_mfma_f32_16x16x32_f16 v[84:87], v[6:9], v[50:53], v[18:21]
	v_mfma_f32_16x16x32_f16 v[88:91], v[10:13], v[50:53], v[38:41]
	ds_read_b128 v[56:59], v75 offset:2048
	ds_read_b128 v[60:63], v75 offset:3072
	v_mfma_f32_16x16x32_f16 v[84:87], v[2:5], v[42:45], v[84:87]
	v_mfma_f32_16x16x32_f16 v[88:91], v[14:17], v[42:45], v[88:91]
	s_waitcnt lgkmcnt(1)
	v_mfma_f32_16x16x32_f16 v[84:87], v[30:33], v[56:59], v[84:87]
	v_mfma_f32_16x16x32_f16 v[88:91], v[22:25], v[56:59], v[88:91]
	s_waitcnt lgkmcnt(0)
	v_mfma_f32_16x16x32_f16 v[84:87], v[34:37], v[60:63], v[84:87]
	v_mfma_f32_16x16x32_f16 v[88:91], v[26:29], v[60:63], v[88:91]
	s_nop 7
	v_exp_f32_e32 v94, v86
	v_exp_f32_e32 v95, v90
	v_exp_f32_e32 v96, v84
	v_exp_f32_e32 v97, v88
	v_exp_f32_e32 v98, v85
	v_exp_f32_e32 v99, v89
	s_setprio 0
	v_pk_add_f32 v[100:101], v[94:95], 1.0 op_sel_hi:[1,0]
	v_pk_fma_f32 v[102:103], v[94:95], s[8:9], v[92:93] op_sel_hi:[1,0,0]
	v_pk_fma_f32 v[100:101], v[96:97], v[100:101], v[100:101]
	v_pk_fma_f32 v[104:105], v[100:101], v[98:99], v[100:101]
	v_rcp_f32_e32 v104, v104
	v_rcp_f32_e32 v105, v105
	v_pk_fma_f32 v[102:103], v[102:103], v[98:99], v[102:103]
	v_pk_fma_f32 v[102:103], v[64:65], v[100:101], v[102:103]
	v_exp_f32_e32 v106, v87
	v_pk_mul_f32 v[64:65], v[102:103], v[104:105]
	v_exp_f32_e32 v108, v64
	v_exp_f32_e32 v109, v65
	v_exp_f32_e32 v107, v91
	v_pk_add_f32 v[110:111], v[108:109], 1.0 op_sel_hi:[1,0]
	v_pk_fma_f32 v[110:111], v[110:111], v[106:107], v[110:111]
	v_rcp_f32_e32 v110, v110
	v_rcp_f32_e32 v111, v111
	v_pk_add_f32 v[112:113], v[108:109], -1.0 op_sel_hi:[1,0]
	v_pk_mul_f32 v[112:113], v[112:113], v[110:111]
	v_cvt_pk_f16_f32 v114, v112, v113
	ds_write_b32 v81, v114 offset:0
	s_waitcnt lgkmcnt(0)
	v_readfirstlane_b32 s10, v67
	v_readfirstlane_b32 s11, v68
	global_load_dword v67, v66, s[0:1] sc1
	global_load_dword v68, v66, s[0:1] offset:4 sc1
	s_min_u32 s10, s10, s11
	s_max_u32 s14, s14, s10
	s_add_u32 s13, s12, 5
	s_min_u32 s13, s13, 450
	s_cmp_ge_u32 s14, s13
	s_cbranch_scc0 .Lca_slow_15
.Lca_ok_13:
	buffer_load_dwordx4 v[42:45], v117, s[4:7], 0 offen offset:2048 sc1
	ds_read_b128 v[50:53], v116 offset:768
	s_setprio 0
	s_waitcnt vmcnt(3) lgkmcnt(0)
	s_setprio 2
	s_barrier
	v_mfma_f32_16x16x32_f16 v[84:87], v[6:9], v[50:53], v[18:21]
	v_mfma_f32_16x16x32_f16 v[88:91], v[10:13], v[50:53], v[38:41]
	ds_read_b128 v[56:59], v75 offset:0
	ds_read_b128 v[60:63], v75 offset:1024
	v_mfma_f32_16x16x32_f16 v[84:87], v[2:5], v[46:49], v[84:87]
	v_mfma_f32_16x16x32_f16 v[88:91], v[14:17], v[46:49], v[88:91]
	s_waitcnt lgkmcnt(1)
	v_mfma_f32_16x16x32_f16 v[84:87], v[30:33], v[56:59], v[84:87]
	v_mfma_f32_16x16x32_f16 v[88:91], v[22:25], v[56:59], v[88:91]
	s_waitcnt lgkmcnt(0)
	v_mfma_f32_16x16x32_f16 v[84:87], v[34:37], v[60:63], v[84:87]
	v_mfma_f32_16x16x32_f16 v[88:91], v[26:29], v[60:63], v[88:91]
	s_nop 7
	v_exp_f32_e32 v94, v86
	v_exp_f32_e32 v95, v90
	v_exp_f32_e32 v96, v84
	v_exp_f32_e32 v97, v88
	v_exp_f32_e32 v98, v85
	v_exp_f32_e32 v99, v89
	s_setprio 0
	v_pk_add_f32 v[100:101], v[94:95], 1.0 op_sel_hi:[1,0]
	v_pk_fma_f32 v[102:103], v[94:95], s[8:9], v[92:93] op_sel_hi:[1,0,0]
	v_pk_fma_f32 v[100:101], v[96:97], v[100:101], v[100:101]
	v_pk_fma_f32 v[104:105], v[100:101], v[98:99], v[100:101]
	v_rcp_f32_e32 v104, v104
	v_rcp_f32_e32 v105, v105
	v_pk_fma_f32 v[102:103], v[102:103], v[98:99], v[102:103]
	v_pk_fma_f32 v[102:103], v[64:65], v[100:101], v[102:103]
	v_exp_f32_e32 v106, v87
	v_pk_mul_f32 v[64:65], v[102:103], v[104:105]
	v_exp_f32_e32 v108, v64
	v_exp_f32_e32 v109, v65
	v_exp_f32_e32 v107, v91
	v_pk_add_f32 v[110:111], v[108:109], 1.0 op_sel_hi:[1,0]
	v_pk_fma_f32 v[110:111], v[110:111], v[106:107], v[110:111]
	v_rcp_f32_e32 v110, v110
	v_rcp_f32_e32 v111, v111
	v_pk_add_f32 v[112:113], v[108:109], -1.0 op_sel_hi:[1,0]
	v_pk_mul_f32 v[112:113], v[112:113], v[110:111]
	v_cvt_pk_f16_f32 v114, v112, v113
	ds_write_b32 v81, v114 offset:2048
	s_waitcnt lgkmcnt(0)
	s_add_u32 s13, s12, 6
	s_min_u32 s13, s13, 450
	s_cmp_ge_u32 s14, s13
	s_cbranch_scc0 .Lca_slow_18
